# GEMM unit end: leading wave-half's re-alignment s_barrier moved from K-loop exit into its epilogue (after store 3/8 FFN_GU, 4/8 MOE_GU, last store in plain epilogues) so its epilogue VALU overlaps the
# baseline (speedup 1.0000x reference)
.LBB0_1349:
	v_lshl_add_u32 v154, s28, 8, v1
	v_lshl_or_b32 v146, s54, 8, v149
	v_ashrrev_i32_e32 v155, 31, v154
	v_ashrrev_i32_e32 v147, 31, v146
	v_lshlrev_b64 v[156:157], 12, v[154:155]
	v_lshl_add_u64 v[156:157], s[2:3], 0, v[156:157]
	v_lshlrev_b64 v[158:159], 1, v[146:147]
	v_lshl_add_u64 v[146:147], v[156:157], 0, v[158:159]
	v_cvt_pk_bf16_f32 v126, v126, v127
	v_cvt_pk_bf16_f32 v127, v128, v129
	v_cvt_pk_bf16_f32 v128, v122, v123
	v_cvt_pk_bf16_f32 v129, v124, v125
	global_store_dwordx4 v[146:147], v[126:129], off
	v_cvt_pk_bf16_f32 v114, v114, v115
	v_cvt_pk_bf16_f32 v115, v116, v117
	v_cvt_pk_bf16_f32 v116, v106, v107
	v_or_b32_e32 v106, 16, v154
	v_ashrrev_i32_e32 v107, 31, v106
	v_lshlrev_b64 v[106:107], 12, v[106:107]
	v_lshl_add_u64 v[106:107], s[2:3], 0, v[106:107]
	v_cvt_pk_bf16_f32 v117, v108, v109
	global_store_dwordx4 v[146:147], v[114:117], off offset:256
	s_nop 1
	v_lshl_add_u64 v[114:115], v[106:107], 0, v[158:159]
	v_cvt_pk_bf16_f32 v106, v118, v119
	v_cvt_pk_bf16_f32 v107, v120, v121
	v_cvt_pk_bf16_f32 v108, v110, v111
	v_cvt_pk_bf16_f32 v109, v112, v113
	global_store_dwordx4 v[114:115], v[106:109], off
	v_cvt_pk_bf16_f32 v98, v98, v99
	v_cvt_pk_bf16_f32 v99, v100, v101
	v_cvt_pk_bf16_f32 v100, v90, v91
	v_or_b32_e32 v90, 32, v154
	v_ashrrev_i32_e32 v91, 31, v90
	v_lshlrev_b64 v[90:91], 12, v[90:91]
	v_lshl_add_u64 v[90:91], s[2:3], 0, v[90:91]
	v_cvt_pk_bf16_f32 v101, v92, v93
	global_store_dwordx4 v[114:115], v[98:101], off offset:256
	s_nop 1
	v_lshl_add_u64 v[98:99], v[90:91], 0, v[158:159]
	v_cvt_pk_bf16_f32 v90, v102, v103
	v_cvt_pk_bf16_f32 v91, v104, v105
	v_cvt_pk_bf16_f32 v92, v94, v95
	v_cvt_pk_bf16_f32 v93, v96, v97
	global_store_dwordx4 v[98:99], v[90:93], off
	v_cvt_pk_bf16_f32 v82, v82, v83
	v_cvt_pk_bf16_f32 v83, v84, v85
	v_cvt_pk_bf16_f32 v84, v74, v75
	v_or_b32_e32 v74, 48, v154
	v_ashrrev_i32_e32 v75, 31, v74
	v_lshlrev_b64 v[74:75], 12, v[74:75]
	v_lshl_add_u64 v[74:75], s[2:3], 0, v[74:75]
	v_cvt_pk_bf16_f32 v85, v76, v77
	global_store_dwordx4 v[98:99], v[82:85], off offset:256
	s_nop 1
	v_lshl_add_u64 v[82:83], v[74:75], 0, v[158:159]
	v_cvt_pk_bf16_f32 v74, v86, v87
	v_cvt_pk_bf16_f32 v75, v88, v89
	v_cvt_pk_bf16_f32 v76, v78, v79
	v_cvt_pk_bf16_f32 v77, v80, v81
	global_store_dwordx4 v[82:83], v[74:77], off
	v_cvt_pk_bf16_f32 v70, v70, v71
	v_cvt_pk_bf16_f32 v71, v72, v73
	v_cvt_pk_bf16_f32 v72, v66, v67
	v_cvt_pk_bf16_f32 v73, v68, v69
	global_store_dwordx4 v[82:83], v[70:73], off offset:256
	v_cvt_pk_bf16_f32 v62, v62, v63
	v_cvt_pk_bf16_f32 v63, v64, v65
	v_cvt_pk_bf16_f32 v64, v58, v59
	v_add_co_u32_e32 v58, vcc, s50, v146
	v_lshl_add_u64 v[66:67], v[146:147], 0, s[4:5]
	s_nop 0
	v_addc_co_u32_e32 v59, vcc, 0, v147, vcc
	v_cvt_pk_bf16_f32 v65, v60, v61
	global_store_dwordx4 v[58:59], v[62:65], off
	v_cvt_pk_bf16_f32 v50, v50, v51
	v_cvt_pk_bf16_f32 v51, v52, v53
	v_cvt_pk_bf16_f32 v52, v42, v43
	v_cvt_pk_bf16_f32 v53, v44, v45
	global_store_dwordx4 v[66:67], v[50:53], off offset:256
	v_cvt_pk_bf16_f32 v42, v54, v55
	v_cvt_pk_bf16_f32 v43, v56, v57
	v_cvt_pk_bf16_f32 v44, v46, v47
	v_add_co_u32_e32 v46, vcc, s51, v146
	s_nop 0
	v_lshl_add_u64 v[50:51], v[146:147], 0, s[14:15]
	v_addc_co_u32_e32 v47, vcc, 0, v147, vcc
	v_cvt_pk_bf16_f32 v45, v48, v49
	global_store_dwordx4 v[46:47], v[42:45], off
	v_cvt_pk_bf16_f32 v34, v34, v35
	v_cvt_pk_bf16_f32 v35, v36, v37
	v_cvt_pk_bf16_f32 v36, v26, v27
	v_cvt_pk_bf16_f32 v37, v28, v29
	global_store_dwordx4 v[50:51], v[34:37], off offset:256
	v_cvt_pk_bf16_f32 v26, v38, v39
	v_cvt_pk_bf16_f32 v27, v40, v41
	v_cvt_pk_bf16_f32 v28, v30, v31
	v_add_co_u32_e32 v30, vcc, s52, v146
	s_nop 0
	v_lshl_add_u64 v[34:35], v[146:147], 0, s[16:17]
	v_addc_co_u32_e32 v31, vcc, 0, v147, vcc
	v_cvt_pk_bf16_f32 v29, v32, v33
	global_store_dwordx4 v[30:31], v[26:29], off
	v_cvt_pk_bf16_f32 v18, v18, v19
	v_cvt_pk_bf16_f32 v19, v20, v21
	v_cvt_pk_bf16_f32 v20, v10, v11
	v_cvt_pk_bf16_f32 v21, v12, v13
	global_store_dwordx4 v[34:35], v[18:21], off offset:256
	v_cvt_pk_bf16_f32 v10, v22, v23
	v_cvt_pk_bf16_f32 v11, v24, v25
	v_cvt_pk_bf16_f32 v12, v14, v15
	v_add_co_u32_e32 v14, vcc, s53, v146
	s_nop 0
	v_lshl_add_u64 v[18:19], v[146:147], 0, s[18:19]
	v_addc_co_u32_e32 v15, vcc, 0, v147, vcc
	s_andn2_b64 vcc, exec, s[8:9]
	s_mov_b64 s[8:9], -1
	v_cvt_pk_bf16_f32 v13, v16, v17
	global_store_dwordx4 v[14:15], v[10:13], off
	v_cvt_pk_bf16_f32 v6, v6, v7
	v_cvt_pk_bf16_f32 v7, v8, v9
	v_cvt_pk_bf16_f32 v8, v2, v3
	v_cvt_pk_bf16_f32 v9, v4, v5
	global_store_dwordx4 v[18:19], v[6:9], off offset:256
	s_cmp_lg_u64 s[12:13], 0
	s_cbranch_scc0 .Lebar_1346
	s_barrier
.Lebar_1346:
	s_cbranch_vccnz .LBB0_1338
	s_andn2_b64 vcc, exec, s[6:7]
	s_cbranch_vccnz .LBB0_1337
	s_barrier
	s_branch .LBB0_1337

.LBB0_1482:
	s_lshl_b32 s26, s26, 8
	s_ashr_i32 s27, s26, 31
	v_lshl_add_u64 v[154:155], s[26:27], 2, v[138:139]
	v_mov_b32_e32 v156, v240
	v_mov_b32_e32 v158, v242
	v_mov_b32_e32 v160, v244
	v_mov_b32_e32 v162, v246
	v_mov_b32_e32 v164, v248
	v_mov_b32_e32 v166, v250
	v_mov_b32_e32 v168, v252
	s_nop 0
	v_mov_b32_e32 v154, v238
	v_lshl_or_b32 v170, s50, 7, v149
	v_add_u32_e32 v153, s26, v1
	v_ashrrev_i32_e32 v171, 31, v170
	s_andn2_b64 vcc, exec, s[8:9]
	s_mov_b64 s[8:9], -1
	v_pk_mul_f32 v[126:127], v[126:127], v[156:157] op_sel_hi:[1,0]
	v_pk_mul_f32 v[128:129], v[128:129], v[156:157] op_sel_hi:[1,0]
	v_pk_mul_f32 v[180:181], v[78:79], v[160:161] op_sel_hi:[1,0]
	v_pk_mul_f32 v[178:179], v[82:83], v[158:159] op_sel_hi:[1,0]
	v_pk_mul_f32 v[78:79], v[44:45], v[164:165] op_sel_hi:[1,0]
	v_pk_mul_f32 v[44:45], v[52:53], v[166:167] op_sel_hi:[1,0]
	v_pk_mul_f32 v[52:53], v[18:19], v[166:167] op_sel_hi:[1,0]
	v_pk_mul_f32 v[18:19], v[126:127], s[14:15] op_sel_hi:[1,0]
	v_pk_mul_f32 v[82:83], v[86:87], v[162:163] op_sel_hi:[1,0]
	v_pk_mul_f32 v[86:87], v[68:69], v[162:163] op_sel_hi:[1,0]
	v_pk_mul_f32 v[68:69], v[34:35], v[164:165] op_sel_hi:[1,0]
	v_pk_mul_f32 v[34:35], v[12:13], v[168:169] op_sel_hi:[1,0]
	v_pk_mul_f32 v[12:13], v[22:23], v[154:155] op_sel_hi:[1,0]
	v_pk_mul_f32 v[22:23], v[128:129], s[14:15] op_sel_hi:[1,0]
	v_exp_f32_e32 v18, v18
	v_exp_f32_e32 v19, v19
	v_exp_f32_e32 v22, v22
	v_exp_f32_e32 v23, v23
	v_pk_mul_f32 v[106:107], v[106:107], v[156:157] op_sel_hi:[1,0]
	v_pk_add_f32 v[18:19], v[18:19], 1.0 op_sel_hi:[1,0]
	v_pk_mul_f32 v[124:125], v[124:125], v[156:157] op_sel_hi:[1,0]
	v_pk_add_f32 v[22:23], v[22:23], 1.0 op_sel_hi:[1,0]
	v_rcp_f32_e32 v18, v18
	v_rcp_f32_e32 v19, v19
	v_rcp_f32_e32 v22, v22
	v_rcp_f32_e32 v23, v23
	v_pk_mul_f32 v[122:123], v[122:123], v[156:157] op_sel_hi:[1,0]
	v_pk_mul_f32 v[108:109], v[108:109], v[156:157] op_sel_hi:[1,0]
	v_pk_mul_f32 v[120:121], v[120:121], v[158:159] op_sel_hi:[1,0]
	v_pk_mul_f32 v[118:119], v[118:119], v[158:159] op_sel_hi:[1,0]
	v_pk_mul_f32 v[116:117], v[116:117], v[158:159] op_sel_hi:[1,0]
	v_pk_mul_f32 v[114:115], v[114:115], v[158:159] op_sel_hi:[1,0]
	v_pk_mul_f32 v[174:175], v[90:91], v[158:159] op_sel_hi:[1,0]
	v_pk_mul_f32 v[176:177], v[92:93], v[158:159] op_sel_hi:[1,0]
	v_pk_mul_f32 v[158:159], v[84:85], v[158:159] op_sel_hi:[1,0]
	v_pk_mul_f32 v[84:85], v[66:67], v[162:163] op_sel_hi:[1,0]
	v_pk_mul_f32 v[66:67], v[58:59], v[164:165] op_sel_hi:[1,0]
	v_pk_mul_f32 v[58:59], v[54:55], v[166:167] op_sel_hi:[1,0]
	v_pk_mul_f32 v[54:55], v[20:21], v[166:167] op_sel_hi:[1,0]
	v_pk_mul_f32 v[20:21], v[40:41], v[168:169] op_sel_hi:[1,0]
	v_pk_mul_f32 v[40:41], v[16:17], v[168:169] op_sel_hi:[1,0]
	v_pk_mul_f32 v[16:17], v[30:31], v[154:155] op_sel_hi:[1,0]
	v_pk_mul_f32 v[30:31], v[126:127], v[106:107]
	v_pk_mul_f32 v[172:173], v[98:99], v[156:157] op_sel_hi:[1,0]
	v_pk_mul_f32 v[156:157], v[100:101], v[156:157] op_sel_hi:[1,0]
	v_pk_mul_f32 v[100:101], v[102:103], v[160:161] op_sel_hi:[1,0]
	v_pk_mul_f32 v[102:103], v[74:75], v[160:161] op_sel_hi:[1,0]
	v_pk_mul_f32 v[92:93], v[94:95], v[162:163] op_sel_hi:[1,0]
	v_pk_mul_f32 v[94:95], v[72:73], v[162:163] op_sel_hi:[1,0]
	v_pk_mul_f32 v[72:73], v[64:65], v[164:165] op_sel_hi:[1,0]
	v_pk_mul_f32 v[74:75], v[62:63], v[164:165] op_sel_hi:[1,0]
	v_pk_mul_f32 v[64:65], v[60:61], v[164:165] op_sel_hi:[1,0]
	v_pk_mul_f32 v[60:61], v[26:27], v[166:167] op_sel_hi:[1,0]
	v_pk_mul_f32 v[62:63], v[28:29], v[166:167] op_sel_hi:[1,0]
	v_pk_mul_f32 v[26:27], v[38:39], v[168:169] op_sel_hi:[1,0]
	v_pk_mul_f32 v[38:39], v[14:15], v[168:169] op_sel_hi:[1,0]
	v_pk_mul_f32 v[28:29], v[10:11], v[168:169] op_sel_hi:[1,0]
	v_pk_mul_f32 v[14:15], v[32:33], v[154:155] op_sel_hi:[1,0]
	v_pk_mul_f32 v[10:11], v[24:25], v[154:155] op_sel_hi:[1,0]
	v_pk_mul_f32 v[24:25], v[128:129], v[108:109]
	v_pk_mul_f32 v[32:33], v[122:123], s[14:15] op_sel_hi:[1,0]
	v_pk_mul_f32 v[18:19], v[30:31], v[18:19]
	v_pk_mul_f32 v[30:31], v[124:125], s[14:15] op_sel_hi:[1,0]
	v_pk_mul_f32 v[22:23], v[24:25], v[22:23]
	v_exp_f32_e32 v24, v32
	v_exp_f32_e32 v25, v33
	v_exp_f32_e32 v30, v30
	v_exp_f32_e32 v31, v31
	v_pk_mul_f32 v[98:99], v[104:105], v[160:161] op_sel_hi:[1,0]
	v_pk_add_f32 v[24:25], v[24:25], 1.0 op_sel_hi:[1,0]
	v_pk_mul_f32 v[104:105], v[76:77], v[160:161] op_sel_hi:[1,0]
	v_pk_add_f32 v[30:31], v[30:31], 1.0 op_sel_hi:[1,0]
	v_rcp_f32_e32 v24, v24
	v_rcp_f32_e32 v25, v25
	v_rcp_f32_e32 v30, v30
	v_rcp_f32_e32 v31, v31
	v_pk_mul_f32 v[76:77], v[42:43], v[164:165] op_sel_hi:[1,0]
	v_pk_mul_f32 v[42:43], v[46:47], v[168:169] op_sel_hi:[1,0]
	v_pk_mul_f32 v[32:33], v[124:125], v[156:157]
	v_pk_mul_f32 v[46:47], v[122:123], v[172:173]
	v_pk_mul_f32 v[90:91], v[96:97], v[162:163] op_sel_hi:[1,0]
	v_pk_mul_f32 v[24:25], v[46:47], v[24:25]
	v_pk_mul_f32 v[46:47], v[32:33], v[30:31]
	v_cvt_pk_bf16_f32 v30, v18, v19
	v_mov_b64_e32 v[18:19], s[6:7]
	v_cvt_pk_bf16_f32 v31, v22, v23
	v_cvt_pk_bf16_f32 v32, v24, v25
	v_mad_i64_i32 v[24:25], s[26:27], v153, s49, v[18:19]
	v_lshlrev_b64 v[22:23], 1, v[170:171]
	v_lshl_add_u64 v[24:25], v[24:25], 0, v[22:23]
	v_cvt_pk_bf16_f32 v33, v46, v47
	global_store_dwordx4 v[24:25], v[30:33], off
	v_pk_mul_f32 v[24:25], v[118:119], s[14:15] op_sel_hi:[1,0]
	v_pk_mul_f32 v[46:47], v[118:119], v[174:175]
	v_pk_mul_f32 v[30:31], v[120:121], s[14:15] op_sel_hi:[1,0]
	v_exp_f32_e32 v24, v24
	v_exp_f32_e32 v30, v30
	v_exp_f32_e32 v31, v31
	v_exp_f32_e32 v25, v25
	v_pk_mul_f32 v[32:33], v[120:121], v[176:177]
	v_pk_mul_f32 v[96:97], v[114:115], v[178:179]
	v_pk_add_f32 v[30:31], v[30:31], 1.0 op_sel_hi:[1,0]
	v_pk_add_f32 v[24:25], v[24:25], 1.0 op_sel_hi:[1,0]
	v_rcp_f32_e32 v30, v30
	v_rcp_f32_e32 v31, v31
	v_rcp_f32_e32 v24, v24
	v_rcp_f32_e32 v25, v25
	v_pk_mul_f32 v[112:113], v[112:113], v[160:161] op_sel_hi:[1,0]
	v_pk_mul_f32 v[32:33], v[32:33], v[30:31]
	v_pk_mul_f32 v[30:31], v[114:115], s[14:15] op_sel_hi:[1,0]
	v_pk_mul_f32 v[24:25], v[46:47], v[24:25]
	v_exp_f32_e32 v30, v30
	v_exp_f32_e32 v31, v31
	v_pk_mul_f32 v[46:47], v[116:117], s[14:15] op_sel_hi:[1,0]
	v_pk_mul_f32 v[182:183], v[80:81], v[160:161] op_sel_hi:[1,0]
	v_exp_f32_e32 v46, v46
	v_exp_f32_e32 v47, v47
	v_pk_add_f32 v[30:31], v[30:31], 1.0 op_sel_hi:[1,0]
	v_pk_mul_f32 v[80:81], v[88:89], v[162:163] op_sel_hi:[1,0]
	v_rcp_f32_e32 v30, v30
	v_rcp_f32_e32 v31, v31
	v_pk_add_f32 v[46:47], v[46:47], 1.0 op_sel_hi:[1,0]
	v_pk_mul_f32 v[88:89], v[70:71], v[162:163] op_sel_hi:[1,0]
	v_rcp_f32_e32 v46, v46
	v_rcp_f32_e32 v47, v47
	v_pk_mul_f32 v[96:97], v[96:97], v[30:31]
	v_cvt_pk_bf16_f32 v30, v24, v25
	v_or_b32_e32 v24, 16, v153
	v_mad_i64_i32 v[24:25], s[26:27], v24, s49, v[18:19]
	v_pk_mul_f32 v[70:71], v[36:37], v[164:165] op_sel_hi:[1,0]
	v_pk_mul_f32 v[36:37], v[48:49], v[168:169] op_sel_hi:[1,0]
	v_pk_mul_f32 v[48:49], v[116:117], v[158:159]
	v_cvt_pk_bf16_f32 v31, v32, v33
	v_lshl_add_u64 v[24:25], v[24:25], 0, v[22:23]
	v_pk_mul_f32 v[46:47], v[48:49], v[46:47]
	v_cvt_pk_bf16_f32 v32, v96, v97
	v_pk_mul_f32 v[110:111], v[110:111], v[160:161] op_sel_hi:[1,0]
	v_cvt_pk_bf16_f32 v33, v46, v47
	global_store_dwordx4 v[24:25], v[30:33], off
	v_pk_mul_f32 v[24:25], v[110:111], s[14:15] op_sel_hi:[1,0]
	v_pk_mul_f32 v[46:47], v[110:111], v[180:181]
	v_pk_mul_f32 v[30:31], v[112:113], s[14:15] op_sel_hi:[1,0]
	v_exp_f32_e32 v24, v24
	v_exp_f32_e32 v30, v30
	v_exp_f32_e32 v31, v31
	v_exp_f32_e32 v25, v25
	v_pk_mul_f32 v[32:33], v[112:113], v[182:183]
	v_pk_mul_f32 v[96:97], v[100:101], v[102:103]
	v_pk_add_f32 v[30:31], v[30:31], 1.0 op_sel_hi:[1,0]
	v_pk_add_f32 v[24:25], v[24:25], 1.0 op_sel_hi:[1,0]
	v_rcp_f32_e32 v30, v30
	v_rcp_f32_e32 v31, v31
	v_rcp_f32_e32 v24, v24
	v_rcp_f32_e32 v25, v25
	v_pk_mul_f32 v[48:49], v[98:99], v[104:105]
	v_pk_mul_f32 v[32:33], v[32:33], v[30:31]
	v_pk_mul_f32 v[30:31], v[100:101], s[14:15] op_sel_hi:[1,0]
	v_pk_mul_f32 v[24:25], v[46:47], v[24:25]
	v_exp_f32_e32 v30, v30
	v_exp_f32_e32 v31, v31
	v_pk_mul_f32 v[46:47], v[98:99], s[14:15] op_sel_hi:[1,0]
	v_pk_mul_f32 v[56:57], v[56:57], v[166:167] op_sel_hi:[1,0]
	v_exp_f32_e32 v46, v46
	v_exp_f32_e32 v47, v47
	v_pk_add_f32 v[30:31], v[30:31], 1.0 op_sel_hi:[1,0]
	v_pk_mul_f32 v[50:51], v[50:51], v[166:167] op_sel_hi:[1,0]
	v_rcp_f32_e32 v30, v30
	v_rcp_f32_e32 v31, v31
	v_pk_add_f32 v[46:47], v[46:47], 1.0 op_sel_hi:[1,0]
	v_pk_mul_f32 v[8:9], v[8:9], v[154:155] op_sel_hi:[1,0]
	v_rcp_f32_e32 v46, v46
	v_rcp_f32_e32 v47, v47
	v_pk_mul_f32 v[96:97], v[96:97], v[30:31]
	v_cvt_pk_bf16_f32 v30, v24, v25
	v_or_b32_e32 v24, 32, v153
	v_mad_i64_i32 v[24:25], s[26:27], v24, s49, v[18:19]
	v_cvt_pk_bf16_f32 v31, v32, v33
	v_lshl_add_u64 v[24:25], v[24:25], 0, v[22:23]
	v_pk_mul_f32 v[46:47], v[48:49], v[46:47]
	v_cvt_pk_bf16_f32 v32, v96, v97
	v_pk_mul_f32 v[48:49], v[80:81], v[86:87]
	v_cvt_pk_bf16_f32 v33, v46, v47
	global_store_dwordx4 v[24:25], v[30:33], off
	s_cmp_lg_u64 s[12:13], 0
	s_cbranch_scc0 .Lebar_1479
	s_barrier
.Lebar_1479:
	v_pk_mul_f32 v[24:25], v[92:93], s[14:15] op_sel_hi:[1,0]
	v_pk_mul_f32 v[46:47], v[92:93], v[88:89]
	v_pk_mul_f32 v[30:31], v[90:91], s[14:15] op_sel_hi:[1,0]
	v_exp_f32_e32 v24, v24
	v_exp_f32_e32 v30, v30
	v_exp_f32_e32 v31, v31
	v_exp_f32_e32 v25, v25
	v_pk_mul_f32 v[32:33], v[90:91], v[94:95]
	v_pk_mul_f32 v[8:9], v[14:15], v[8:9]
	v_pk_add_f32 v[30:31], v[30:31], 1.0 op_sel_hi:[1,0]
	v_pk_add_f32 v[24:25], v[24:25], 1.0 op_sel_hi:[1,0]
	v_rcp_f32_e32 v30, v30
	v_rcp_f32_e32 v31, v31
	v_rcp_f32_e32 v24, v24
	v_rcp_f32_e32 v25, v25
	v_pk_mul_f32 v[6:7], v[6:7], v[154:155] op_sel_hi:[1,0]
	v_pk_mul_f32 v[32:33], v[32:33], v[30:31]
	v_pk_mul_f32 v[30:31], v[82:83], s[14:15] op_sel_hi:[1,0]
	v_pk_mul_f32 v[24:25], v[46:47], v[24:25]
	v_exp_f32_e32 v30, v30
	v_exp_f32_e32 v31, v31
	v_pk_mul_f32 v[46:47], v[80:81], s[14:15] op_sel_hi:[1,0]
	v_pk_mul_f32 v[80:81], v[82:83], v[84:85]
	v_exp_f32_e32 v46, v46
	v_exp_f32_e32 v47, v47
	v_pk_add_f32 v[30:31], v[30:31], 1.0 op_sel_hi:[1,0]
	v_pk_mul_f32 v[6:7], v[16:17], v[6:7]
	v_rcp_f32_e32 v30, v30
	v_rcp_f32_e32 v31, v31
	v_pk_add_f32 v[46:47], v[46:47], 1.0 op_sel_hi:[1,0]
	v_pk_mul_f32 v[2:3], v[2:3], v[154:155] op_sel_hi:[1,0]
	v_rcp_f32_e32 v46, v46
	v_rcp_f32_e32 v47, v47
	v_pk_mul_f32 v[80:81], v[80:81], v[30:31]
	v_cvt_pk_bf16_f32 v30, v24, v25
	v_or_b32_e32 v24, 48, v153
	v_mad_i64_i32 v[24:25], s[26:27], v24, s49, v[18:19]
	v_cvt_pk_bf16_f32 v31, v32, v33
	v_lshl_add_u64 v[24:25], v[24:25], 0, v[22:23]
	v_pk_mul_f32 v[46:47], v[48:49], v[46:47]
	v_cvt_pk_bf16_f32 v32, v80, v81
	v_add_u32_e32 v80, 0x80, v153
	v_cvt_pk_bf16_f32 v33, v46, v47
	global_store_dwordx4 v[24:25], v[30:33], off
	v_pk_mul_f32 v[24:25], v[74:75], s[14:15] op_sel_hi:[1,0]
	v_pk_mul_f32 v[46:47], v[74:75], v[76:77]
	v_pk_mul_f32 v[30:31], v[72:73], s[14:15] op_sel_hi:[1,0]
	v_exp_f32_e32 v24, v24
	v_exp_f32_e32 v30, v30
	v_exp_f32_e32 v31, v31
	v_exp_f32_e32 v25, v25
	v_pk_mul_f32 v[32:33], v[72:73], v[78:79]
	v_pk_mul_f32 v[48:49], v[64:65], v[70:71]
	v_pk_add_f32 v[30:31], v[30:31], 1.0 op_sel_hi:[1,0]
	v_pk_add_f32 v[24:25], v[24:25], 1.0 op_sel_hi:[1,0]
	v_rcp_f32_e32 v30, v30
	v_rcp_f32_e32 v31, v31
	v_rcp_f32_e32 v24, v24
	v_rcp_f32_e32 v25, v25
	v_pk_mul_f32 v[4:5], v[4:5], v[154:155] op_sel_hi:[1,0]
	v_pk_mul_f32 v[32:33], v[32:33], v[30:31]
	v_pk_mul_f32 v[30:31], v[66:67], s[14:15] op_sel_hi:[1,0]
	v_pk_mul_f32 v[24:25], v[46:47], v[24:25]
	v_exp_f32_e32 v30, v30
	v_exp_f32_e32 v31, v31
	v_pk_mul_f32 v[46:47], v[64:65], s[14:15] op_sel_hi:[1,0]
	v_pk_mul_f32 v[64:65], v[66:67], v[68:69]
	v_exp_f32_e32 v46, v46
	v_exp_f32_e32 v47, v47
	v_pk_add_f32 v[30:31], v[30:31], 1.0 op_sel_hi:[1,0]
	v_pk_mul_f32 v[2:3], v[12:13], v[2:3]
	v_rcp_f32_e32 v30, v30
	v_rcp_f32_e32 v31, v31
	v_pk_add_f32 v[46:47], v[46:47], 1.0 op_sel_hi:[1,0]
	v_pk_mul_f32 v[4:5], v[10:11], v[4:5]
	v_rcp_f32_e32 v46, v46
	v_rcp_f32_e32 v47, v47
	v_pk_mul_f32 v[64:65], v[64:65], v[30:31]
	v_cvt_pk_bf16_f32 v30, v24, v25
	v_mad_i64_i32 v[24:25], s[26:27], v80, s49, v[18:19]
	v_cvt_pk_bf16_f32 v31, v32, v33
	v_lshl_add_u64 v[24:25], v[24:25], 0, v[22:23]
	v_pk_mul_f32 v[46:47], v[48:49], v[46:47]
	v_cvt_pk_bf16_f32 v32, v64, v65
	v_pk_mul_f32 v[48:49], v[50:51], v[52:53]
	v_cvt_pk_bf16_f32 v33, v46, v47
	global_store_dwordx4 v[24:25], v[30:33], off
	v_pk_mul_f32 v[24:25], v[58:59], s[14:15] op_sel_hi:[1,0]
	v_pk_mul_f32 v[46:47], v[58:59], v[60:61]
	v_pk_mul_f32 v[30:31], v[56:57], s[14:15] op_sel_hi:[1,0]
	v_exp_f32_e32 v24, v24
	v_exp_f32_e32 v30, v30
	v_exp_f32_e32 v31, v31
	v_exp_f32_e32 v25, v25
	v_pk_mul_f32 v[32:33], v[56:57], v[62:63]
	v_pk_add_f32 v[30:31], v[30:31], 1.0 op_sel_hi:[1,0]
	s_nop 0
	v_rcp_f32_e32 v30, v30
	v_rcp_f32_e32 v31, v31
	v_pk_add_f32 v[24:25], v[24:25], 1.0 op_sel_hi:[1,0]
	v_pk_mul_f32 v[32:33], v[32:33], v[30:31]
	v_rcp_f32_e32 v24, v24
	v_rcp_f32_e32 v25, v25
	v_pk_mul_f32 v[30:31], v[50:51], s[14:15] op_sel_hi:[1,0]
	v_pk_mul_f32 v[24:25], v[46:47], v[24:25]
	v_exp_f32_e32 v30, v30
	v_exp_f32_e32 v31, v31
	v_pk_mul_f32 v[46:47], v[44:45], s[14:15] op_sel_hi:[1,0]
	v_pk_mul_f32 v[44:45], v[44:45], v[54:55]
	v_exp_f32_e32 v46, v46
	v_exp_f32_e32 v47, v47
	v_pk_add_f32 v[30:31], v[30:31], 1.0 op_sel_hi:[1,0]
	v_pk_add_f32 v[46:47], v[46:47], 1.0 op_sel_hi:[1,0]
	v_rcp_f32_e32 v30, v30
	v_rcp_f32_e32 v31, v31
	v_rcp_f32_e32 v46, v46
	v_rcp_f32_e32 v47, v47
	v_pk_mul_f32 v[48:49], v[48:49], v[30:31]
	v_cvt_pk_bf16_f32 v30, v24, v25
	v_add_u32_e32 v24, 0x90, v153
	v_mad_i64_i32 v[24:25], s[26:27], v24, s49, v[18:19]
	v_cvt_pk_bf16_f32 v31, v32, v33
	v_lshl_add_u64 v[24:25], v[24:25], 0, v[22:23]
	v_pk_mul_f32 v[44:45], v[44:45], v[46:47]
	v_cvt_pk_bf16_f32 v32, v48, v49
	s_nop 0
	v_cvt_pk_bf16_f32 v33, v44, v45
	global_store_dwordx4 v[24:25], v[30:33], off
	v_pk_mul_f32 v[24:25], v[42:43], s[14:15] op_sel_hi:[1,0]
	s_nop 0
	v_pk_mul_f32 v[30:31], v[36:37], s[14:15] op_sel_hi:[1,0]
	v_exp_f32_e32 v24, v24
	v_exp_f32_e32 v25, v25
	v_exp_f32_e32 v30, v30
	v_exp_f32_e32 v31, v31
	v_pk_mul_f32 v[32:33], v[36:37], v[40:41]
	v_pk_add_f32 v[24:25], v[24:25], 1.0 op_sel_hi:[1,0]
	v_pk_mul_f32 v[36:37], v[42:43], v[38:39]
	v_pk_add_f32 v[30:31], v[30:31], 1.0 op_sel_hi:[1,0]
	v_rcp_f32_e32 v24, v24
	v_rcp_f32_e32 v25, v25
	v_rcp_f32_e32 v30, v30
	v_rcp_f32_e32 v31, v31
	v_pk_mul_f32 v[24:25], v[36:37], v[24:25]
	v_pk_mul_f32 v[36:37], v[20:21], s[14:15] op_sel_hi:[1,0]
	v_pk_mul_f32 v[30:31], v[32:33], v[30:31]
	v_pk_mul_f32 v[32:33], v[26:27], s[14:15] op_sel_hi:[1,0]
	v_exp_f32_e32 v36, v36
	v_exp_f32_e32 v32, v32
	v_exp_f32_e32 v33, v33
	v_exp_f32_e32 v37, v37
	v_pk_mul_f32 v[20:21], v[20:21], v[34:35]
	v_pk_mul_f32 v[26:27], v[26:27], v[28:29]
	v_pk_add_f32 v[32:33], v[32:33], 1.0 op_sel_hi:[1,0]
	v_pk_add_f32 v[36:37], v[36:37], 1.0 op_sel_hi:[1,0]
	v_rcp_f32_e32 v32, v32
	v_rcp_f32_e32 v33, v33
	v_rcp_f32_e32 v36, v36
	v_rcp_f32_e32 v37, v37
	v_cvt_pk_bf16_f32 v24, v24, v25
	v_pk_mul_f32 v[26:27], v[26:27], v[32:33]
	v_cvt_pk_bf16_f32 v25, v30, v31
	v_pk_mul_f32 v[20:21], v[20:21], v[36:37]
	v_cvt_pk_bf16_f32 v26, v26, v27
	s_nop 0
	v_cvt_pk_bf16_f32 v27, v20, v21
	v_add_u32_e32 v20, 0xa0, v153
	v_mad_i64_i32 v[20:21], s[26:27], v20, s49, v[18:19]
	v_lshl_add_u64 v[20:21], v[20:21], 0, v[22:23]
	global_store_dwordx4 v[20:21], v[24:27], off
	v_pk_mul_f32 v[20:21], v[16:17], s[14:15] op_sel_hi:[1,0]
	v_pk_mul_f32 v[16:17], v[10:11], s[14:15] op_sel_hi:[1,0]
	v_exp_f32_e32 v20, v20
	v_exp_f32_e32 v21, v21
	v_pk_mul_f32 v[24:25], v[14:15], s[14:15] op_sel_hi:[1,0]
	v_pk_mul_f32 v[14:15], v[12:13], s[14:15] op_sel_hi:[1,0]
	v_exp_f32_e32 v24, v24
	v_exp_f32_e32 v14, v14
	v_exp_f32_e32 v15, v15
	v_exp_f32_e32 v25, v25
	v_pk_add_f32 v[20:21], v[20:21], 1.0 op_sel_hi:[1,0]
	v_exp_f32_e32 v16, v16
	v_exp_f32_e32 v17, v17
	v_rcp_f32_e32 v20, v20
	v_rcp_f32_e32 v21, v21
	v_pk_add_f32 v[14:15], v[14:15], 1.0 op_sel_hi:[1,0]
	v_pk_add_f32 v[24:25], v[24:25], 1.0 op_sel_hi:[1,0]
	v_rcp_f32_e32 v14, v14
	v_rcp_f32_e32 v15, v15
	v_pk_add_f32 v[16:17], v[16:17], 1.0 op_sel_hi:[1,0]
	v_rcp_f32_e32 v24, v24
	v_rcp_f32_e32 v25, v25
	v_pk_mul_f32 v[6:7], v[6:7], v[20:21]
	v_rcp_f32_e32 v16, v16
	v_rcp_f32_e32 v17, v17
	v_pk_mul_f32 v[10:11], v[2:3], v[14:15]
	v_cvt_pk_bf16_f32 v2, v6, v7
	v_add_u32_e32 v6, 0xb0, v153
	v_mad_i64_i32 v[6:7], s[26:27], v6, s49, v[18:19]
	v_lshl_add_u64 v[6:7], v[6:7], 0, v[22:23]
	v_pk_mul_f32 v[8:9], v[8:9], v[24:25]
	v_pk_mul_f32 v[12:13], v[4:5], v[16:17]
	v_cvt_pk_bf16_f32 v3, v8, v9
	v_cvt_pk_bf16_f32 v4, v10, v11
	s_nop 0
	v_cvt_pk_bf16_f32 v5, v12, v13
	global_store_dwordx4 v[6:7], v[2:5], off
	s_cbranch_vccnz .LBB0_1475
	s_andn2_b64 vcc, exec, s[4:5]
	s_cbranch_vccnz .LBB0_1474
	s_barrier
	s_branch .LBB0_1474

.LBB0_1565:
	v_lshl_add_u32 v154, s55, 8, v1
	v_lshl_or_b32 v146, s56, 8, v149
	v_ashrrev_i32_e32 v155, 31, v154
	v_ashrrev_i32_e32 v147, 31, v146
	v_lshlrev_b64 v[156:157], 12, v[154:155]
	v_lshl_add_u64 v[156:157], s[2:3], 0, v[156:157]
	v_lshlrev_b64 v[158:159], 1, v[146:147]
	v_lshl_add_u64 v[146:147], v[156:157], 0, v[158:159]
	v_cvt_pk_bf16_f32 v126, v126, v127
	v_cvt_pk_bf16_f32 v127, v128, v129
	v_cvt_pk_bf16_f32 v128, v122, v123
	v_cvt_pk_bf16_f32 v129, v124, v125
	global_store_dwordx4 v[146:147], v[126:129], off
	v_cvt_pk_bf16_f32 v114, v114, v115
	v_cvt_pk_bf16_f32 v115, v116, v117
	v_cvt_pk_bf16_f32 v116, v106, v107
	v_or_b32_e32 v106, 16, v154
	v_ashrrev_i32_e32 v107, 31, v106
	v_lshlrev_b64 v[106:107], 12, v[106:107]
	v_lshl_add_u64 v[106:107], s[2:3], 0, v[106:107]
	v_cvt_pk_bf16_f32 v117, v108, v109
	global_store_dwordx4 v[146:147], v[114:117], off offset:256
	s_nop 1
	v_lshl_add_u64 v[114:115], v[106:107], 0, v[158:159]
	v_cvt_pk_bf16_f32 v106, v118, v119
	v_cvt_pk_bf16_f32 v107, v120, v121
	v_cvt_pk_bf16_f32 v108, v110, v111
	v_cvt_pk_bf16_f32 v109, v112, v113
	global_store_dwordx4 v[114:115], v[106:109], off
	v_cvt_pk_bf16_f32 v98, v98, v99
	v_cvt_pk_bf16_f32 v99, v100, v101
	v_cvt_pk_bf16_f32 v100, v90, v91
	v_or_b32_e32 v90, 32, v154
	v_ashrrev_i32_e32 v91, 31, v90
	v_lshlrev_b64 v[90:91], 12, v[90:91]
	v_lshl_add_u64 v[90:91], s[2:3], 0, v[90:91]
	v_cvt_pk_bf16_f32 v101, v92, v93
	global_store_dwordx4 v[114:115], v[98:101], off offset:256
	s_nop 1
	v_lshl_add_u64 v[98:99], v[90:91], 0, v[158:159]
	v_cvt_pk_bf16_f32 v90, v102, v103
	v_cvt_pk_bf16_f32 v91, v104, v105
	v_cvt_pk_bf16_f32 v92, v94, v95
	v_cvt_pk_bf16_f32 v93, v96, v97
	global_store_dwordx4 v[98:99], v[90:93], off
	v_cvt_pk_bf16_f32 v82, v82, v83
	v_cvt_pk_bf16_f32 v83, v84, v85
	v_cvt_pk_bf16_f32 v84, v74, v75
	v_or_b32_e32 v74, 48, v154
	v_ashrrev_i32_e32 v75, 31, v74
	v_lshlrev_b64 v[74:75], 12, v[74:75]
	v_lshl_add_u64 v[74:75], s[2:3], 0, v[74:75]
	v_cvt_pk_bf16_f32 v85, v76, v77
	global_store_dwordx4 v[98:99], v[82:85], off offset:256
	s_nop 1
	v_lshl_add_u64 v[82:83], v[74:75], 0, v[158:159]
	v_cvt_pk_bf16_f32 v74, v86, v87
	v_cvt_pk_bf16_f32 v75, v88, v89
	v_cvt_pk_bf16_f32 v76, v78, v79
	v_cvt_pk_bf16_f32 v77, v80, v81
	global_store_dwordx4 v[82:83], v[74:77], off
	v_cvt_pk_bf16_f32 v70, v70, v71
	v_cvt_pk_bf16_f32 v71, v72, v73
	v_cvt_pk_bf16_f32 v72, v66, v67
	v_cvt_pk_bf16_f32 v73, v68, v69
	global_store_dwordx4 v[82:83], v[70:73], off offset:256
	v_cvt_pk_bf16_f32 v62, v62, v63
	v_cvt_pk_bf16_f32 v63, v64, v65
	v_cvt_pk_bf16_f32 v64, v58, v59
	v_add_co_u32_e32 v58, vcc, s49, v146
	v_lshl_add_u64 v[66:67], v[146:147], 0, s[14:15]
	s_nop 0
	v_addc_co_u32_e32 v59, vcc, 0, v147, vcc
	v_cvt_pk_bf16_f32 v65, v60, v61
	global_store_dwordx4 v[58:59], v[62:65], off
	v_cvt_pk_bf16_f32 v50, v50, v51
	v_cvt_pk_bf16_f32 v51, v52, v53
	v_cvt_pk_bf16_f32 v52, v42, v43
	v_cvt_pk_bf16_f32 v53, v44, v45
	global_store_dwordx4 v[66:67], v[50:53], off offset:256
	v_cvt_pk_bf16_f32 v42, v54, v55
	v_cvt_pk_bf16_f32 v43, v56, v57
	v_cvt_pk_bf16_f32 v44, v46, v47
	v_add_co_u32_e32 v46, vcc, s50, v146
	s_nop 0
	v_lshl_add_u64 v[50:51], v[146:147], 0, s[16:17]
	v_addc_co_u32_e32 v47, vcc, 0, v147, vcc
	v_cvt_pk_bf16_f32 v45, v48, v49
	global_store_dwordx4 v[46:47], v[42:45], off
	v_cvt_pk_bf16_f32 v34, v34, v35
	v_cvt_pk_bf16_f32 v35, v36, v37
	v_cvt_pk_bf16_f32 v36, v26, v27
	v_cvt_pk_bf16_f32 v37, v28, v29
	global_store_dwordx4 v[50:51], v[34:37], off offset:256
	v_cvt_pk_bf16_f32 v26, v38, v39
	v_cvt_pk_bf16_f32 v27, v40, v41
	v_cvt_pk_bf16_f32 v28, v30, v31
	v_add_co_u32_e32 v30, vcc, s51, v146
	s_nop 0
	v_lshl_add_u64 v[34:35], v[146:147], 0, s[18:19]
	v_addc_co_u32_e32 v31, vcc, 0, v147, vcc
	v_cvt_pk_bf16_f32 v29, v32, v33
	global_store_dwordx4 v[30:31], v[26:29], off
	v_cvt_pk_bf16_f32 v18, v18, v19
	v_cvt_pk_bf16_f32 v19, v20, v21
	v_cvt_pk_bf16_f32 v20, v10, v11
	v_cvt_pk_bf16_f32 v21, v12, v13
	global_store_dwordx4 v[34:35], v[18:21], off offset:256
	v_cvt_pk_bf16_f32 v10, v22, v23
	v_cvt_pk_bf16_f32 v11, v24, v25
	v_cvt_pk_bf16_f32 v12, v14, v15
	v_add_co_u32_e32 v14, vcc, s52, v146
	s_nop 0
	v_lshl_add_u64 v[18:19], v[146:147], 0, s[22:23]
	v_addc_co_u32_e32 v15, vcc, 0, v147, vcc
	s_and_b64 vcc, exec, s[8:9]
	s_mov_b64 s[8:9], -1
	v_cvt_pk_bf16_f32 v13, v16, v17
	global_store_dwordx4 v[14:15], v[10:13], off
	v_cvt_pk_bf16_f32 v6, v6, v7
	v_cvt_pk_bf16_f32 v7, v8, v9
	v_cvt_pk_bf16_f32 v8, v2, v3
	v_cvt_pk_bf16_f32 v9, v4, v5
	global_store_dwordx4 v[18:19], v[6:9], off offset:256
	s_cmp_lg_u64 s[12:13], 0
	s_cbranch_scc0 .Lebar_1562
	s_barrier

.LBB0_2117:
	v_lshl_add_u32 v154, s30, 8, v1
	v_lshl_or_b32 v146, s56, 8, v149
	v_ashrrev_i32_e32 v155, 31, v154
	v_ashrrev_i32_e32 v147, 31, v146
	v_lshlrev_b64 v[156:157], 12, v[154:155]
	v_lshl_add_u64 v[156:157], s[2:3], 0, v[156:157]
	v_lshlrev_b64 v[158:159], 1, v[146:147]
	v_lshl_add_u64 v[146:147], v[156:157], 0, v[158:159]
	v_cvt_pk_bf16_f32 v126, v126, v127
	v_cvt_pk_bf16_f32 v127, v128, v129
	v_cvt_pk_bf16_f32 v128, v122, v123
	v_cvt_pk_bf16_f32 v129, v124, v125
	global_store_dwordx4 v[146:147], v[126:129], off
	v_cvt_pk_bf16_f32 v114, v114, v115
	v_cvt_pk_bf16_f32 v115, v116, v117
	v_cvt_pk_bf16_f32 v116, v106, v107
	v_or_b32_e32 v106, 16, v154
	v_ashrrev_i32_e32 v107, 31, v106
	v_lshlrev_b64 v[106:107], 12, v[106:107]
	v_lshl_add_u64 v[106:107], s[2:3], 0, v[106:107]
	v_cvt_pk_bf16_f32 v117, v108, v109
	global_store_dwordx4 v[146:147], v[114:117], off offset:256
	s_nop 1
	v_lshl_add_u64 v[114:115], v[106:107], 0, v[158:159]
	v_cvt_pk_bf16_f32 v106, v118, v119
	v_cvt_pk_bf16_f32 v107, v120, v121
	v_cvt_pk_bf16_f32 v108, v110, v111
	v_cvt_pk_bf16_f32 v109, v112, v113
	global_store_dwordx4 v[114:115], v[106:109], off
	v_cvt_pk_bf16_f32 v98, v98, v99
	v_cvt_pk_bf16_f32 v99, v100, v101
	v_cvt_pk_bf16_f32 v100, v90, v91
	v_or_b32_e32 v90, 32, v154
	v_ashrrev_i32_e32 v91, 31, v90
	v_lshlrev_b64 v[90:91], 12, v[90:91]
	v_lshl_add_u64 v[90:91], s[2:3], 0, v[90:91]
	v_cvt_pk_bf16_f32 v101, v92, v93
	global_store_dwordx4 v[114:115], v[98:101], off offset:256
	s_nop 1
	v_lshl_add_u64 v[98:99], v[90:91], 0, v[158:159]
	v_cvt_pk_bf16_f32 v90, v102, v103
	v_cvt_pk_bf16_f32 v91, v104, v105
	v_cvt_pk_bf16_f32 v92, v94, v95
	v_cvt_pk_bf16_f32 v93, v96, v97
	global_store_dwordx4 v[98:99], v[90:93], off
	v_cvt_pk_bf16_f32 v82, v82, v83
	v_cvt_pk_bf16_f32 v83, v84, v85
	v_cvt_pk_bf16_f32 v84, v74, v75
	v_or_b32_e32 v74, 48, v154
	v_ashrrev_i32_e32 v75, 31, v74
	v_lshlrev_b64 v[74:75], 12, v[74:75]
	v_lshl_add_u64 v[74:75], s[2:3], 0, v[74:75]
	v_cvt_pk_bf16_f32 v85, v76, v77
	global_store_dwordx4 v[98:99], v[82:85], off offset:256
	s_nop 1
	v_lshl_add_u64 v[82:83], v[74:75], 0, v[158:159]
	v_cvt_pk_bf16_f32 v74, v86, v87
	v_cvt_pk_bf16_f32 v75, v88, v89
	v_cvt_pk_bf16_f32 v76, v78, v79
	v_cvt_pk_bf16_f32 v77, v80, v81
	global_store_dwordx4 v[82:83], v[74:77], off
	v_cvt_pk_bf16_f32 v70, v70, v71
	v_cvt_pk_bf16_f32 v71, v72, v73
	v_cvt_pk_bf16_f32 v72, v66, v67
	v_cvt_pk_bf16_f32 v73, v68, v69
	global_store_dwordx4 v[82:83], v[70:73], off offset:256
	v_cvt_pk_bf16_f32 v62, v62, v63
	v_cvt_pk_bf16_f32 v63, v64, v65
	v_cvt_pk_bf16_f32 v64, v58, v59
	v_add_co_u32_e32 v58, vcc, s52, v146
	v_lshl_add_u64 v[66:67], v[146:147], 0, s[6:7]
	s_nop 0
	v_addc_co_u32_e32 v59, vcc, 0, v147, vcc
	v_cvt_pk_bf16_f32 v65, v60, v61
	global_store_dwordx4 v[58:59], v[62:65], off
	v_cvt_pk_bf16_f32 v50, v50, v51
	v_cvt_pk_bf16_f32 v51, v52, v53
	v_cvt_pk_bf16_f32 v52, v42, v43
	v_cvt_pk_bf16_f32 v53, v44, v45
	global_store_dwordx4 v[66:67], v[50:53], off offset:256
	v_cvt_pk_bf16_f32 v42, v54, v55
	v_cvt_pk_bf16_f32 v43, v56, v57
	v_cvt_pk_bf16_f32 v44, v46, v47
	v_add_co_u32_e32 v46, vcc, s53, v146
	s_nop 0
	v_lshl_add_u64 v[50:51], v[146:147], 0, s[14:15]
	v_addc_co_u32_e32 v47, vcc, 0, v147, vcc
	v_cvt_pk_bf16_f32 v45, v48, v49
	global_store_dwordx4 v[46:47], v[42:45], off
	v_cvt_pk_bf16_f32 v34, v34, v35
	v_cvt_pk_bf16_f32 v35, v36, v37
	v_cvt_pk_bf16_f32 v36, v26, v27
	v_cvt_pk_bf16_f32 v37, v28, v29
	global_store_dwordx4 v[50:51], v[34:37], off offset:256
	v_cvt_pk_bf16_f32 v26, v38, v39
	v_cvt_pk_bf16_f32 v27, v40, v41
	v_cvt_pk_bf16_f32 v28, v30, v31
	v_add_co_u32_e32 v30, vcc, s54, v146
	s_nop 0
	v_lshl_add_u64 v[34:35], v[146:147], 0, s[16:17]
	v_addc_co_u32_e32 v31, vcc, 0, v147, vcc
	v_cvt_pk_bf16_f32 v29, v32, v33
	global_store_dwordx4 v[30:31], v[26:29], off
	v_cvt_pk_bf16_f32 v18, v18, v19
	v_cvt_pk_bf16_f32 v19, v20, v21
	v_cvt_pk_bf16_f32 v20, v10, v11
	v_cvt_pk_bf16_f32 v21, v12, v13
	global_store_dwordx4 v[34:35], v[18:21], off offset:256
	v_cvt_pk_bf16_f32 v10, v22, v23
	v_cvt_pk_bf16_f32 v11, v24, v25
	v_cvt_pk_bf16_f32 v12, v14, v15
	v_add_co_u32_e32 v14, vcc, s55, v146
	s_nop 0
	v_lshl_add_u64 v[18:19], v[146:147], 0, s[18:19]
	v_addc_co_u32_e32 v15, vcc, 0, v147, vcc
	s_andn2_b64 vcc, exec, s[4:5]
	s_mov_b64 s[4:5], -1
	v_cvt_pk_bf16_f32 v13, v16, v17
	global_store_dwordx4 v[14:15], v[10:13], off
	v_cvt_pk_bf16_f32 v6, v6, v7
	v_cvt_pk_bf16_f32 v7, v8, v9
	v_cvt_pk_bf16_f32 v8, v2, v3
	v_cvt_pk_bf16_f32 v9, v4, v5
	global_store_dwordx4 v[18:19], v[6:9], off offset:256
	s_cmp_lg_u64 s[12:13], 0
	s_cbranch_scc0 .Lebar_2114
	s_barrier
.Lebar_2114:
	s_cbranch_vccnz .LBB0_2106
	s_andn2_b64 vcc, exec, s[8:9]
	s_cbranch_vccnz .LBB0_2105
	s_barrier
	s_branch .LBB0_2105

.LBB0_2369:
	v_pk_mul_f32 v[8:9], v[160:161], s[6:7] op_sel_hi:[1,0]
	v_pk_mul_f32 v[4:5], v[158:159], s[6:7] op_sel_hi:[1,0]
	v_exp_f32_e32 v8, v8
	v_exp_f32_e32 v9, v9
	v_exp_f32_e32 v4, v4
	v_exp_f32_e32 v5, v5
	v_pk_mul_f32 v[10:11], v[160:161], v[156:157]
	v_pk_fma_f32 v[8:9], v[8:9], s[18:19], s[18:19] op_sel_hi:[1,0,0]
	v_pk_mul_f32 v[12:13], v[158:159], v[154:155]
	v_pk_fma_f32 v[4:5], v[4:5], s[18:19], s[18:19] op_sel_hi:[1,0,0]
	v_rcp_f32_e32 v8, v8
	v_rcp_f32_e32 v9, v9
	v_rcp_f32_e32 v4, v4
	v_rcp_f32_e32 v5, v5
	v_pk_mul_f32 v[16:17], v[150:151], v[146:147]
	v_pk_mul_f32 v[8:9], v[10:11], v[8:9]
	v_pk_mul_f32 v[10:11], v[150:151], s[6:7] op_sel_hi:[1,0]
	v_pk_mul_f32 v[4:5], v[12:13], v[4:5]
	v_exp_f32_e32 v10, v10
	v_exp_f32_e32 v11, v11
	v_pk_mul_f32 v[12:13], v[152:153], s[6:7] op_sel_hi:[1,0]
	v_pk_mul_f32 v[14:15], v[152:153], v[148:149]
	v_exp_f32_e32 v12, v12
	v_exp_f32_e32 v13, v13
	v_pk_fma_f32 v[10:11], v[10:11], s[18:19], s[18:19] op_sel_hi:[1,0,0]
	v_med3_f32 v4, v4, s62, v191
	v_rcp_f32_e32 v10, v10
	v_rcp_f32_e32 v11, v11
	v_pk_fma_f32 v[12:13], v[12:13], s[18:19], s[18:19] op_sel_hi:[1,0,0]
	v_med3_f32 v5, v5, s62, v191
	v_rcp_f32_e32 v12, v12
	v_rcp_f32_e32 v13, v13
	v_pk_mul_f32 v[10:11], v[16:17], v[10:11]
	v_med3_f32 v7, v8, s62, v191
	v_mov_b32_e32 v8, 0
	v_pk_mul_f32 v[12:13], v[14:15], v[12:13]
	v_med3_f32 v14, v9, s62, v191
	v_cvt_pk_fp8_f32 v8, v4, v5
	v_med3_f32 v4, v10, s62, v191
	v_med3_f32 v5, v11, s62, v191
	v_mov_b32_e32 v9, 0
	v_cvt_pk_fp8_f32 v9, v4, v5
	v_med3_f32 v4, v12, s62, v191
	v_med3_f32 v5, v13, s62, v191
	v_cvt_pk_fp8_f32 v8, v7, v14 op_sel:[0,0,1]
	v_cvt_pk_fp8_f32 v9, v4, v5 op_sel:[0,0,1]
	v_lshl_add_u32 v6, s30, 8, v1
	v_lshl_or_b32 v2, s65, 7, v185
	v_mov_b64_e32 v[4:5], s[10:11]
	v_ashrrev_i32_e32 v3, 31, v2
	v_mad_i64_i32 v[10:11], s[34:35], v6, s63, v[4:5]
	v_lshl_add_u64 v[10:11], v[10:11], 0, v[2:3]
	s_nop 15
	s_nop 15
	global_store_dwordx2 v[10:11], v[8:9], off
	v_pk_mul_f32 v[10:11], v[144:145], s[6:7] op_sel_hi:[1,0]
	v_pk_mul_f32 v[8:9], v[142:143], s[6:7] op_sel_hi:[1,0]
	v_exp_f32_e32 v10, v10
	v_exp_f32_e32 v11, v11
	v_exp_f32_e32 v8, v8
	v_exp_f32_e32 v9, v9
	v_pk_mul_f32 v[12:13], v[144:145], v[140:141]
	v_pk_fma_f32 v[10:11], v[10:11], s[18:19], s[18:19] op_sel_hi:[1,0,0]
	v_pk_mul_f32 v[14:15], v[142:143], v[138:139]
	v_rcp_f32_e32 v10, v10
	v_rcp_f32_e32 v11, v11
	v_pk_fma_f32 v[8:9], v[8:9], s[18:19], s[18:19] op_sel_hi:[1,0,0]
	v_pk_mul_f32 v[18:19], v[134:135], v[130:131]
	v_rcp_f32_e32 v8, v8
	v_rcp_f32_e32 v9, v9
	v_pk_mul_f32 v[10:11], v[12:13], v[10:11]
	v_pk_mul_f32 v[12:13], v[134:135], s[6:7] op_sel_hi:[1,0]
	v_pk_mul_f32 v[16:17], v[136:137], v[132:133]
	v_exp_f32_e32 v12, v12
	v_exp_f32_e32 v13, v13
	v_pk_mul_f32 v[8:9], v[14:15], v[8:9]
	v_pk_mul_f32 v[14:15], v[136:137], s[6:7] op_sel_hi:[1,0]
	v_med3_f32 v7, v8, s62, v191
	v_exp_f32_e32 v14, v14
	v_exp_f32_e32 v15, v15
	v_pk_fma_f32 v[12:13], v[12:13], s[18:19], s[18:19] op_sel_hi:[1,0,0]
	v_med3_f32 v9, v9, s62, v191
	v_rcp_f32_e32 v12, v12
	v_rcp_f32_e32 v13, v13
	v_pk_fma_f32 v[14:15], v[14:15], s[18:19], s[18:19] op_sel_hi:[1,0,0]
	v_mov_b32_e32 v8, 0
	v_rcp_f32_e32 v14, v14
	v_rcp_f32_e32 v15, v15
	v_pk_mul_f32 v[12:13], v[18:19], v[12:13]
	v_cvt_pk_fp8_f32 v8, v7, v9
	v_med3_f32 v7, v12, s62, v191
	v_med3_f32 v12, v13, s62, v191
	v_mov_b32_e32 v9, 0
	v_cvt_pk_fp8_f32 v9, v7, v12
	v_pk_mul_f32 v[14:15], v[16:17], v[14:15]
	v_med3_f32 v10, v10, s62, v191
	v_med3_f32 v11, v11, s62, v191
	v_cvt_pk_fp8_f32 v8, v10, v11 op_sel:[0,0,1]
	v_med3_f32 v7, v14, s62, v191
	v_med3_f32 v10, v15, s62, v191
	v_cvt_pk_fp8_f32 v9, v7, v10 op_sel:[0,0,1]
	v_or_b32_e32 v7, 16, v6
	v_mad_i64_i32 v[10:11], s[34:35], v7, s63, v[4:5]
	v_lshl_add_u64 v[10:11], v[10:11], 0, v[2:3]
	global_store_dwordx2 v[10:11], v[8:9], off
	v_pk_mul_f32 v[10:11], v[128:129], s[6:7] op_sel_hi:[1,0]
	v_pk_mul_f32 v[8:9], v[126:127], s[6:7] op_sel_hi:[1,0]
	v_exp_f32_e32 v10, v10
	v_exp_f32_e32 v11, v11
	v_exp_f32_e32 v8, v8
	v_exp_f32_e32 v9, v9
	v_pk_mul_f32 v[12:13], v[128:129], v[124:125]
	v_pk_fma_f32 v[10:11], v[10:11], s[18:19], s[18:19] op_sel_hi:[1,0,0]
	v_pk_mul_f32 v[14:15], v[126:127], v[122:123]
	v_rcp_f32_e32 v10, v10
	v_rcp_f32_e32 v11, v11
	v_pk_fma_f32 v[8:9], v[8:9], s[18:19], s[18:19] op_sel_hi:[1,0,0]
	v_pk_mul_f32 v[18:19], v[118:119], v[114:115]
	v_rcp_f32_e32 v8, v8
	v_rcp_f32_e32 v9, v9
	v_pk_mul_f32 v[10:11], v[12:13], v[10:11]
	v_pk_mul_f32 v[12:13], v[118:119], s[6:7] op_sel_hi:[1,0]
	v_pk_mul_f32 v[16:17], v[120:121], v[116:117]
	v_exp_f32_e32 v12, v12
	v_exp_f32_e32 v13, v13
	v_pk_mul_f32 v[8:9], v[14:15], v[8:9]
	v_pk_mul_f32 v[14:15], v[120:121], s[6:7] op_sel_hi:[1,0]
	v_med3_f32 v7, v8, s62, v191
	v_exp_f32_e32 v14, v14
	v_exp_f32_e32 v15, v15
	v_pk_fma_f32 v[12:13], v[12:13], s[18:19], s[18:19] op_sel_hi:[1,0,0]
	v_med3_f32 v9, v9, s62, v191
	v_rcp_f32_e32 v12, v12
	v_rcp_f32_e32 v13, v13
	v_pk_fma_f32 v[14:15], v[14:15], s[18:19], s[18:19] op_sel_hi:[1,0,0]
	v_mov_b32_e32 v8, 0
	v_rcp_f32_e32 v14, v14
	v_rcp_f32_e32 v15, v15
	v_pk_mul_f32 v[12:13], v[18:19], v[12:13]
	v_cvt_pk_fp8_f32 v8, v7, v9
	v_med3_f32 v7, v12, s62, v191
	v_med3_f32 v12, v13, s62, v191
	v_mov_b32_e32 v9, 0
	v_cvt_pk_fp8_f32 v9, v7, v12
	v_pk_mul_f32 v[14:15], v[16:17], v[14:15]
	v_med3_f32 v10, v10, s62, v191
	v_med3_f32 v11, v11, s62, v191
	v_cvt_pk_fp8_f32 v8, v10, v11 op_sel:[0,0,1]
	v_med3_f32 v7, v14, s62, v191
	v_med3_f32 v10, v15, s62, v191
	v_cvt_pk_fp8_f32 v9, v7, v10 op_sel:[0,0,1]
	v_or_b32_e32 v7, 32, v6
	v_mad_i64_i32 v[10:11], s[34:35], v7, s63, v[4:5]
	v_lshl_add_u64 v[10:11], v[10:11], 0, v[2:3]
	global_store_dwordx2 v[10:11], v[8:9], off
	v_pk_mul_f32 v[10:11], v[112:113], s[6:7] op_sel_hi:[1,0]
	v_pk_mul_f32 v[8:9], v[110:111], s[6:7] op_sel_hi:[1,0]
	v_exp_f32_e32 v10, v10
	v_exp_f32_e32 v11, v11
	v_exp_f32_e32 v8, v8
	v_exp_f32_e32 v9, v9
	v_pk_mul_f32 v[12:13], v[112:113], v[108:109]
	v_pk_fma_f32 v[10:11], v[10:11], s[18:19], s[18:19] op_sel_hi:[1,0,0]
	v_pk_mul_f32 v[14:15], v[110:111], v[106:107]
	v_rcp_f32_e32 v10, v10
	v_rcp_f32_e32 v11, v11
	v_pk_fma_f32 v[8:9], v[8:9], s[18:19], s[18:19] op_sel_hi:[1,0,0]
	v_pk_mul_f32 v[18:19], v[102:103], v[98:99]
	v_rcp_f32_e32 v8, v8
	v_rcp_f32_e32 v9, v9
	v_pk_mul_f32 v[10:11], v[12:13], v[10:11]
	v_pk_mul_f32 v[12:13], v[102:103], s[6:7] op_sel_hi:[1,0]
	v_pk_mul_f32 v[16:17], v[104:105], v[100:101]
	v_exp_f32_e32 v12, v12
	v_exp_f32_e32 v13, v13
	v_pk_mul_f32 v[8:9], v[14:15], v[8:9]
	v_pk_mul_f32 v[14:15], v[104:105], s[6:7] op_sel_hi:[1,0]
	v_med3_f32 v7, v8, s62, v191
	v_exp_f32_e32 v14, v14
	v_exp_f32_e32 v15, v15
	v_pk_fma_f32 v[12:13], v[12:13], s[18:19], s[18:19] op_sel_hi:[1,0,0]
	v_med3_f32 v9, v9, s62, v191
	v_rcp_f32_e32 v12, v12
	v_rcp_f32_e32 v13, v13
	v_pk_fma_f32 v[14:15], v[14:15], s[18:19], s[18:19] op_sel_hi:[1,0,0]
	v_mov_b32_e32 v8, 0
	v_rcp_f32_e32 v14, v14
	v_rcp_f32_e32 v15, v15
	v_pk_mul_f32 v[12:13], v[18:19], v[12:13]
	v_cvt_pk_fp8_f32 v8, v7, v9
	v_med3_f32 v7, v12, s62, v191
	v_med3_f32 v12, v13, s62, v191
	v_mov_b32_e32 v9, 0
	v_cvt_pk_fp8_f32 v9, v7, v12
	v_pk_mul_f32 v[14:15], v[16:17], v[14:15]
	v_med3_f32 v10, v10, s62, v191
	v_med3_f32 v11, v11, s62, v191
	v_cvt_pk_fp8_f32 v8, v10, v11 op_sel:[0,0,1]
	v_med3_f32 v7, v14, s62, v191
	v_med3_f32 v10, v15, s62, v191
	v_cvt_pk_fp8_f32 v9, v7, v10 op_sel:[0,0,1]
	v_or_b32_e32 v7, 48, v6
	v_mad_i64_i32 v[10:11], s[34:35], v7, s63, v[4:5]
	v_lshl_add_u64 v[10:11], v[10:11], 0, v[2:3]
	global_store_dwordx2 v[10:11], v[8:9], off
	s_cmp_lg_u64 s[16:17], 0
	s_cbranch_scc0 .Lebar_2366
	s_barrier
.Lebar_2366:
	v_pk_mul_f32 v[8:9], v[94:95], s[6:7] op_sel_hi:[1,0]
	v_pk_mul_f32 v[10:11], v[96:97], s[6:7] op_sel_hi:[1,0]
	v_exp_f32_e32 v8, v8
	v_exp_f32_e32 v9, v9
	v_exp_f32_e32 v10, v10
	v_exp_f32_e32 v11, v11
	v_pk_mul_f32 v[12:13], v[96:97], v[92:93]
	v_pk_fma_f32 v[8:9], v[8:9], s[18:19], s[18:19] op_sel_hi:[1,0,0]
	v_pk_mul_f32 v[14:15], v[94:95], v[90:91]
	v_pk_fma_f32 v[10:11], v[10:11], s[18:19], s[18:19] op_sel_hi:[1,0,0]
	v_rcp_f32_e32 v8, v8
	v_rcp_f32_e32 v9, v9
	v_rcp_f32_e32 v10, v10
	v_rcp_f32_e32 v11, v11
	v_pk_mul_f32 v[16:17], v[88:89], v[84:85]
	v_pk_mul_f32 v[8:9], v[14:15], v[8:9]
	v_pk_mul_f32 v[14:15], v[88:89], s[6:7] op_sel_hi:[1,0]
	v_pk_mul_f32 v[10:11], v[12:13], v[10:11]
	v_pk_mul_f32 v[12:13], v[86:87], s[6:7] op_sel_hi:[1,0]
	v_exp_f32_e32 v14, v14
	v_exp_f32_e32 v12, v12
	v_exp_f32_e32 v13, v13
	v_exp_f32_e32 v15, v15
	v_pk_mul_f32 v[18:19], v[86:87], v[82:83]
	v_med3_f32 v9, v9, s62, v191
	v_pk_fma_f32 v[12:13], v[12:13], s[18:19], s[18:19] op_sel_hi:[1,0,0]
	v_pk_fma_f32 v[14:15], v[14:15], s[18:19], s[18:19] op_sel_hi:[1,0,0]
	v_rcp_f32_e32 v12, v12
	v_rcp_f32_e32 v13, v13
	v_rcp_f32_e32 v14, v14
	v_rcp_f32_e32 v15, v15
	v_med3_f32 v10, v10, s62, v191
	v_pk_mul_f32 v[12:13], v[18:19], v[12:13]
	v_med3_f32 v11, v11, s62, v191
	v_pk_mul_f32 v[14:15], v[16:17], v[14:15]
	v_med3_f32 v16, v8, s62, v191
	v_mov_b32_e32 v8, 0
	v_cvt_pk_fp8_f32 v8, v16, v9
	v_med3_f32 v12, v12, s62, v191
	v_med3_f32 v13, v13, s62, v191
	v_mov_b32_e32 v9, 0
	v_cvt_pk_fp8_f32 v9, v12, v13
	v_cvt_pk_fp8_f32 v8, v10, v11 op_sel:[0,0,1]
	v_med3_f32 v10, v14, s62, v191
	v_med3_f32 v11, v15, s62, v191
	v_cvt_pk_fp8_f32 v9, v10, v11 op_sel:[0,0,1]
	v_add_u32_e32 v7, 0x80, v6
	v_mad_i64_i32 v[10:11], s[34:35], v7, s63, v[4:5]
	v_lshl_add_u64 v[10:11], v[10:11], 0, v[2:3]
	global_store_dwordx2 v[10:11], v[8:9], off
	v_pk_mul_f32 v[10:11], v[80:81], s[6:7] op_sel_hi:[1,0]
	v_pk_mul_f32 v[8:9], v[78:79], s[6:7] op_sel_hi:[1,0]
	v_exp_f32_e32 v10, v10
	v_exp_f32_e32 v11, v11
	v_exp_f32_e32 v8, v8
	v_exp_f32_e32 v9, v9
	v_pk_mul_f32 v[12:13], v[80:81], v[76:77]
	v_pk_fma_f32 v[10:11], v[10:11], s[18:19], s[18:19] op_sel_hi:[1,0,0]
	v_pk_mul_f32 v[14:15], v[78:79], v[74:75]
	v_rcp_f32_e32 v10, v10
	v_rcp_f32_e32 v11, v11
	v_pk_fma_f32 v[8:9], v[8:9], s[18:19], s[18:19] op_sel_hi:[1,0,0]
	v_pk_mul_f32 v[18:19], v[70:71], v[66:67]
	v_rcp_f32_e32 v8, v8
	v_rcp_f32_e32 v9, v9
	v_pk_mul_f32 v[10:11], v[12:13], v[10:11]
	v_pk_mul_f32 v[12:13], v[70:71], s[6:7] op_sel_hi:[1,0]
	v_pk_mul_f32 v[16:17], v[72:73], v[68:69]
	v_exp_f32_e32 v12, v12
	v_exp_f32_e32 v13, v13
	v_pk_mul_f32 v[8:9], v[14:15], v[8:9]
	v_pk_mul_f32 v[14:15], v[72:73], s[6:7] op_sel_hi:[1,0]
	v_med3_f32 v7, v8, s62, v191
	v_exp_f32_e32 v14, v14
	v_exp_f32_e32 v15, v15
	v_pk_fma_f32 v[12:13], v[12:13], s[18:19], s[18:19] op_sel_hi:[1,0,0]
	v_med3_f32 v9, v9, s62, v191
	v_rcp_f32_e32 v12, v12
	v_rcp_f32_e32 v13, v13
	v_pk_fma_f32 v[14:15], v[14:15], s[18:19], s[18:19] op_sel_hi:[1,0,0]
	v_mov_b32_e32 v8, 0
	v_rcp_f32_e32 v14, v14
	v_rcp_f32_e32 v15, v15
	v_pk_mul_f32 v[12:13], v[18:19], v[12:13]
	v_cvt_pk_fp8_f32 v8, v7, v9
	v_med3_f32 v7, v12, s62, v191
	v_med3_f32 v12, v13, s62, v191
	v_mov_b32_e32 v9, 0
	v_cvt_pk_fp8_f32 v9, v7, v12
	v_pk_mul_f32 v[14:15], v[16:17], v[14:15]
	v_med3_f32 v10, v10, s62, v191
	v_med3_f32 v11, v11, s62, v191
	v_cvt_pk_fp8_f32 v8, v10, v11 op_sel:[0,0,1]
	v_med3_f32 v7, v14, s62, v191
	v_med3_f32 v10, v15, s62, v191
	v_cvt_pk_fp8_f32 v9, v7, v10 op_sel:[0,0,1]
	v_add_u32_e32 v7, 0x90, v6
	v_mad_i64_i32 v[10:11], s[34:35], v7, s63, v[4:5]
	v_lshl_add_u64 v[10:11], v[10:11], 0, v[2:3]
	global_store_dwordx2 v[10:11], v[8:9], off
	v_pk_mul_f32 v[10:11], v[64:65], s[6:7] op_sel_hi:[1,0]
	v_pk_mul_f32 v[8:9], v[62:63], s[6:7] op_sel_hi:[1,0]
	v_exp_f32_e32 v10, v10
	v_exp_f32_e32 v11, v11
	v_exp_f32_e32 v8, v8
	v_exp_f32_e32 v9, v9
	v_pk_mul_f32 v[12:13], v[64:65], v[60:61]
	v_pk_fma_f32 v[10:11], v[10:11], s[18:19], s[18:19] op_sel_hi:[1,0,0]
	v_pk_mul_f32 v[14:15], v[62:63], v[58:59]
	v_rcp_f32_e32 v10, v10
	v_rcp_f32_e32 v11, v11
	v_pk_fma_f32 v[8:9], v[8:9], s[18:19], s[18:19] op_sel_hi:[1,0,0]
	v_pk_mul_f32 v[18:19], v[54:55], v[50:51]
	v_rcp_f32_e32 v8, v8
	v_rcp_f32_e32 v9, v9
	v_pk_mul_f32 v[10:11], v[12:13], v[10:11]
	v_pk_mul_f32 v[12:13], v[54:55], s[6:7] op_sel_hi:[1,0]
	v_pk_mul_f32 v[16:17], v[56:57], v[52:53]
	v_exp_f32_e32 v12, v12
	v_exp_f32_e32 v13, v13
	v_pk_mul_f32 v[8:9], v[14:15], v[8:9]
	v_pk_mul_f32 v[14:15], v[56:57], s[6:7] op_sel_hi:[1,0]
	v_med3_f32 v7, v8, s62, v191
	v_exp_f32_e32 v14, v14
	v_exp_f32_e32 v15, v15
	v_pk_fma_f32 v[12:13], v[12:13], s[18:19], s[18:19] op_sel_hi:[1,0,0]
	v_med3_f32 v9, v9, s62, v191
	v_rcp_f32_e32 v12, v12
	v_rcp_f32_e32 v13, v13
	v_pk_fma_f32 v[14:15], v[14:15], s[18:19], s[18:19] op_sel_hi:[1,0,0]
	v_mov_b32_e32 v8, 0
	v_rcp_f32_e32 v14, v14
	v_rcp_f32_e32 v15, v15
	v_pk_mul_f32 v[12:13], v[18:19], v[12:13]
	v_cvt_pk_fp8_f32 v8, v7, v9
	v_med3_f32 v7, v12, s62, v191
	v_med3_f32 v12, v13, s62, v191
	v_mov_b32_e32 v9, 0
	v_cvt_pk_fp8_f32 v9, v7, v12
	v_pk_mul_f32 v[14:15], v[16:17], v[14:15]
	v_med3_f32 v10, v10, s62, v191
	v_med3_f32 v11, v11, s62, v191
	v_cvt_pk_fp8_f32 v8, v10, v11 op_sel:[0,0,1]
	v_med3_f32 v7, v14, s62, v191
	v_med3_f32 v10, v15, s62, v191
	v_cvt_pk_fp8_f32 v9, v7, v10 op_sel:[0,0,1]
	v_add_u32_e32 v7, 0xa0, v6
	v_mad_i64_i32 v[10:11], s[34:35], v7, s63, v[4:5]
	v_lshl_add_u64 v[10:11], v[10:11], 0, v[2:3]
	global_store_dwordx2 v[10:11], v[8:9], off
	v_pk_mul_f32 v[10:11], v[48:49], s[6:7] op_sel_hi:[1,0]
	v_pk_mul_f32 v[8:9], v[46:47], s[6:7] op_sel_hi:[1,0]
	v_exp_f32_e32 v10, v10
	v_exp_f32_e32 v11, v11
	v_exp_f32_e32 v8, v8
	v_exp_f32_e32 v9, v9
	v_pk_mul_f32 v[12:13], v[48:49], v[44:45]
	v_pk_fma_f32 v[10:11], v[10:11], s[18:19], s[18:19] op_sel_hi:[1,0,0]
	v_pk_mul_f32 v[14:15], v[46:47], v[42:43]
	v_rcp_f32_e32 v10, v10
	v_rcp_f32_e32 v11, v11
	v_pk_fma_f32 v[8:9], v[8:9], s[18:19], s[18:19] op_sel_hi:[1,0,0]
	v_pk_mul_f32 v[18:19], v[38:39], v[34:35]
	v_rcp_f32_e32 v8, v8
	v_rcp_f32_e32 v9, v9
	v_pk_mul_f32 v[10:11], v[12:13], v[10:11]
	v_pk_mul_f32 v[12:13], v[38:39], s[6:7] op_sel_hi:[1,0]
	v_pk_mul_f32 v[16:17], v[40:41], v[36:37]
	v_exp_f32_e32 v12, v12
	v_exp_f32_e32 v13, v13
	v_pk_mul_f32 v[8:9], v[14:15], v[8:9]
	v_pk_mul_f32 v[14:15], v[40:41], s[6:7] op_sel_hi:[1,0]
	v_med3_f32 v7, v8, s62, v191
	v_exp_f32_e32 v14, v14
	v_exp_f32_e32 v15, v15
	v_pk_fma_f32 v[12:13], v[12:13], s[18:19], s[18:19] op_sel_hi:[1,0,0]
	v_med3_f32 v9, v9, s62, v191
	v_rcp_f32_e32 v12, v12
	v_rcp_f32_e32 v13, v13
	v_pk_fma_f32 v[14:15], v[14:15], s[18:19], s[18:19] op_sel_hi:[1,0,0]
	v_mov_b32_e32 v8, 0
	v_rcp_f32_e32 v14, v14
	v_rcp_f32_e32 v15, v15
	v_pk_mul_f32 v[12:13], v[18:19], v[12:13]
	v_cvt_pk_fp8_f32 v8, v7, v9
	v_med3_f32 v7, v12, s62, v191
	v_med3_f32 v12, v13, s62, v191
	v_mov_b32_e32 v9, 0
	v_cvt_pk_fp8_f32 v9, v7, v12
	v_pk_mul_f32 v[14:15], v[16:17], v[14:15]
	v_med3_f32 v10, v10, s62, v191
	v_med3_f32 v11, v11, s62, v191
	v_cvt_pk_fp8_f32 v8, v10, v11 op_sel:[0,0,1]
	v_med3_f32 v7, v14, s62, v191
	v_med3_f32 v10, v15, s62, v191
	v_cvt_pk_fp8_f32 v9, v7, v10 op_sel:[0,0,1]
	v_add_u32_e32 v6, 0xb0, v6
	v_mad_i64_i32 v[4:5], s[34:35], v6, s63, v[4:5]
	v_lshl_add_u64 v[2:3], v[4:5], 0, v[2:3]
	s_andn2_b64 vcc, exec, s[4:5]
	s_mov_b64 s[4:5], -1
	s_mov_b32 s66, s74
	global_store_dwordx2 v[2:3], v[8:9], off
	s_cbranch_vccnz .LBB0_2362
	s_andn2_b64 vcc, exec, s[8:9]
	s_cbranch_vccnz .LBB0_2361
	s_barrier
	s_branch .LBB0_2361

.LBB0_2444:
	v_lshl_add_u32 v6, s70, 8, v188
	v_lshl_or_b32 v0, s69, 8, v190
	v_ashrrev_i32_e32 v7, 31, v6
	v_ashrrev_i32_e32 v1, 31, v0
	v_lshlrev_b64 v[2:3], 12, v[6:7]
	v_lshl_add_u64 v[2:3], s[16:17], 0, v[2:3]
	v_lshlrev_b64 v[8:9], 1, v[0:1]
	s_nop 15
	s_nop 15
	v_lshl_add_u64 v[0:1], v[2:3], 0, v[8:9]
	v_cvt_pk_bf16_f32 v2, v156, v157
	v_cvt_pk_bf16_f32 v3, v158, v159
	v_cvt_pk_bf16_f32 v4, v152, v153
	v_cvt_pk_bf16_f32 v5, v154, v155
	global_store_dwordx4 v[0:1], v[2:5], off
	s_nop 1
	v_cvt_pk_bf16_f32 v2, v144, v145
	v_cvt_pk_bf16_f32 v3, v146, v147
	v_cvt_pk_bf16_f32 v4, v136, v137
	v_cvt_pk_bf16_f32 v5, v138, v139
	global_store_dwordx4 v[0:1], v[2:5], off offset:256
	s_nop 1
	v_or_b32_e32 v2, 16, v6
	v_ashrrev_i32_e32 v3, 31, v2
	v_lshlrev_b64 v[2:3], 12, v[2:3]
	v_lshl_add_u64 v[2:3], s[16:17], 0, v[2:3]
	v_lshl_add_u64 v[10:11], v[2:3], 0, v[8:9]
	v_cvt_pk_bf16_f32 v2, v148, v149
	v_cvt_pk_bf16_f32 v3, v150, v151
	v_cvt_pk_bf16_f32 v4, v140, v141
	v_cvt_pk_bf16_f32 v5, v142, v143
	global_store_dwordx4 v[10:11], v[2:5], off
	s_nop 1
	v_cvt_pk_bf16_f32 v2, v128, v129
	v_cvt_pk_bf16_f32 v3, v130, v131
	v_cvt_pk_bf16_f32 v4, v120, v121
	v_cvt_pk_bf16_f32 v5, v122, v123
	global_store_dwordx4 v[10:11], v[2:5], off offset:256
	s_nop 1
	v_or_b32_e32 v2, 32, v6
	v_ashrrev_i32_e32 v3, 31, v2
	v_lshlrev_b64 v[2:3], 12, v[2:3]
	v_lshl_add_u64 v[2:3], s[16:17], 0, v[2:3]
	v_lshl_add_u64 v[10:11], v[2:3], 0, v[8:9]
	v_cvt_pk_bf16_f32 v2, v132, v133
	v_cvt_pk_bf16_f32 v3, v134, v135
	v_cvt_pk_bf16_f32 v4, v124, v125
	v_cvt_pk_bf16_f32 v5, v126, v127
	global_store_dwordx4 v[10:11], v[2:5], off
	s_nop 1
	v_cvt_pk_bf16_f32 v2, v112, v113
	v_cvt_pk_bf16_f32 v3, v114, v115
	v_cvt_pk_bf16_f32 v4, v104, v105
	v_cvt_pk_bf16_f32 v5, v106, v107
	global_store_dwordx4 v[10:11], v[2:5], off offset:256
	s_nop 1
	v_or_b32_e32 v2, 48, v6
	v_ashrrev_i32_e32 v3, 31, v2
	v_lshlrev_b64 v[2:3], 12, v[2:3]
	v_lshl_add_u64 v[2:3], s[16:17], 0, v[2:3]
	v_lshl_add_u64 v[6:7], v[2:3], 0, v[8:9]
	v_cvt_pk_bf16_f32 v2, v116, v117
	v_cvt_pk_bf16_f32 v3, v118, v119
	v_cvt_pk_bf16_f32 v4, v108, v109
	v_cvt_pk_bf16_f32 v5, v110, v111
	global_store_dwordx4 v[6:7], v[2:5], off
	v_add_co_u32_e32 v8, vcc, s63, v0
	s_nop 0
	v_cvt_pk_bf16_f32 v2, v100, v101
	v_cvt_pk_bf16_f32 v3, v102, v103
	v_cvt_pk_bf16_f32 v4, v96, v97
	v_cvt_pk_bf16_f32 v5, v98, v99
	global_store_dwordx4 v[6:7], v[2:5], off offset:256
	v_addc_co_u32_e32 v9, vcc, 0, v1, vcc
	s_nop 0
	v_cvt_pk_bf16_f32 v2, v92, v93
	v_cvt_pk_bf16_f32 v3, v94, v95
	v_cvt_pk_bf16_f32 v4, v88, v89
	v_cvt_pk_bf16_f32 v5, v90, v91
	v_lshl_add_u64 v[6:7], v[0:1], 0, s[28:29]
	global_store_dwordx4 v[8:9], v[2:5], off
	v_add_co_u32_e32 v8, vcc, s64, v0
	s_nop 0
	v_cvt_pk_bf16_f32 v2, v80, v81
	v_cvt_pk_bf16_f32 v3, v82, v83
	v_cvt_pk_bf16_f32 v4, v72, v73
	v_cvt_pk_bf16_f32 v5, v74, v75
	global_store_dwordx4 v[6:7], v[2:5], off offset:256
	v_addc_co_u32_e32 v9, vcc, 0, v1, vcc
	s_nop 0
	v_cvt_pk_bf16_f32 v2, v84, v85
	v_cvt_pk_bf16_f32 v3, v86, v87
	v_cvt_pk_bf16_f32 v4, v76, v77
	v_cvt_pk_bf16_f32 v5, v78, v79
	v_lshl_add_u64 v[6:7], v[0:1], 0, s[30:31]
	global_store_dwordx4 v[8:9], v[2:5], off
	v_add_co_u32_e32 v8, vcc, s65, v0
	s_nop 0
	v_cvt_pk_bf16_f32 v2, v64, v65
	v_cvt_pk_bf16_f32 v3, v66, v67
	v_cvt_pk_bf16_f32 v4, v56, v57
	v_cvt_pk_bf16_f32 v5, v58, v59
	global_store_dwordx4 v[6:7], v[2:5], off offset:256
	v_lshl_add_u64 v[6:7], v[0:1], 0, s[34:35]
	v_addc_co_u32_e32 v9, vcc, 0, v1, vcc
	v_cvt_pk_bf16_f32 v2, v68, v69
	v_cvt_pk_bf16_f32 v3, v70, v71
	v_cvt_pk_bf16_f32 v4, v60, v61
	v_cvt_pk_bf16_f32 v5, v62, v63
	global_store_dwordx4 v[8:9], v[2:5], off
	s_nop 1
	v_cvt_pk_bf16_f32 v2, v48, v49
	v_cvt_pk_bf16_f32 v3, v50, v51
	v_cvt_pk_bf16_f32 v4, v40, v41
	v_cvt_pk_bf16_f32 v5, v42, v43
	global_store_dwordx4 v[6:7], v[2:5], off offset:256
	v_lshl_add_u64 v[6:7], v[0:1], 0, s[36:37]
	v_add_co_u32_e32 v0, vcc, s66, v0
	v_cvt_pk_bf16_f32 v2, v52, v53
	v_cvt_pk_bf16_f32 v3, v54, v55
	v_cvt_pk_bf16_f32 v4, v44, v45
	v_cvt_pk_bf16_f32 v5, v46, v47
	s_nop 1
	v_addc_co_u32_e32 v1, vcc, 0, v1, vcc
	s_and_b64 vcc, exec, s[4:5]
	s_mov_b64 s[4:5], -1
	global_store_dwordx4 v[0:1], v[2:5], off
	v_cvt_pk_bf16_f32 v0, v36, v37
	v_cvt_pk_bf16_f32 v1, v38, v39
	s_nop 1
	v_cvt_pk_bf16_f32 v2, v32, v33
	v_cvt_pk_bf16_f32 v3, v34, v35
	global_store_dwordx4 v[6:7], v[0:3], off offset:256
	s_cmp_lg_u64 s[24:25], 0
	s_cbranch_scc0 .Lebar_2441
	s_barrier
.Lebar_2441:
	s_cbranch_vccnz .LBB0_2433
	s_andn2_b64 vcc, exec, s[12:13]
	s_cbranch_vccnz .LBB0_2432
	s_barrier
	s_branch .LBB0_2432
